# static priority for waves 0-3 during phase 4 only (the half whose P.V runs in the same tile)
# speedup vs baseline: 1.0078x; 1.0078x over previous
.LBB0_796:
	s_andn2_b64 vcc, exec, s[4:5]
	s_cbranch_vccnz .LBB0_902
	v_cmp_lt_u32_e32 vcc, 255, v0
	s_cbranch_vccnz .Lp4prio_skip
	s_setprio 1
